# in_proj phase-start stagger retuned (s_sleep 0x41 -> 0x30) after the tile-boundary changes
# speedup vs baseline: 1.0024x; 1.0007x over previous
.LBB0_535:
	s_add_i32 s0, s0, -1
	s_cmp_eq_u32 s0, 0
	s_sleep 0x30
	s_cbranch_scc0 .LBB0_535
